# swap_prio2_l3
# speedup vs baseline: 1.0057x; 1.0057x over previous
.LBB3_8:
	s_cmp_eq_u32 s90, 0
	s_cbranch_scc1 .Lrec2_p_lo
	s_setprio 3
